# speedup vs baseline: 1.0195x; 1.0111x over previous
.LBB1_8:
	s_or_b64 exec, exec, s[4:5]
	s_waitcnt vmcnt(1)
	v_mov_b32_e32 v184, 1
	v_lshl_add_u32 v180, v176, 2, v172
	v_lshl_add_u32 v181, v177, 2, v172
	v_lshl_add_u32 v182, v178, 2, v172
	v_lshl_add_u32 v183, v179, 2, v172
	ds_add_u32 v180, v184
	ds_add_u32 v181, v184
	ds_add_u32 v182, v184
	ds_add_u32 v183, v184
	s_waitcnt lgkmcnt(0)
	ds_read_b32 v151, v173
	s_waitcnt lgkmcnt(0)
	v_cvt_f32_i32_e32 v185, v151
	ds_write_b32 v173, v185 offset:256
	v_add_u32_e32 v10, v172, v2
	v_readfirstlane_b32 s4, v0
	s_waitcnt vmcnt(1) lgkmcnt(0)
	s_cmpk_lt_u32 s4, 0x100
	s_cbranch_scc1 .Lprio_done
	s_setprio 1
.Lprio_done:
	s_barrier
	ds_read_b128 v[18:21], v10 offset:256
	ds_read_b128 v[22:25], v10 offset:288
	ds_read_b128 v[82:85], v10 offset:320
	ds_read_b128 v[86:89], v10 offset:352
	ds_read_b128 v[74:77], v10 offset:384
	ds_read_b128 v[78:81], v10 offset:416
	ds_read_b128 v[2:5], v213 offset:32768
	ds_read_b128 v[6:9], v213 offset:0
	ds_read_b128 v[66:69], v10 offset:448
	ds_read_b128 v[70:73], v10 offset:480
	ds_read_b128 v[10:13], v213 offset:1024
	s_waitcnt lgkmcnt(3)
	v_pk_mul_f32 v[26:27], v[8:9], v[20:21]
	v_pk_mul_f32 v[28:29], v[6:7], v[18:19]
	ds_read_b128 v[14:17], v213 offset:8192
	s_waitcnt lgkmcnt(1)
	v_pk_mul_f32 v[12:13], v[12:13], v[24:25]
	v_pk_mul_f32 v[10:11], v[10:11], v[22:23]
	v_pk_fma_f32 v[30:31], v[8:9], v[20:21], v[12:13]
	v_pk_fma_f32 v[32:33], v[6:7], v[18:19], v[10:11]
	v_cvt_pk_bf16_f32 v9, v12, v13
	v_cvt_pk_bf16_f32 v7, v26, v27
	v_cvt_pk_bf16_f32 v8, v10, v11
	v_cvt_pk_bf16_f32 v6, v28, v29
	ds_read_b128 v[10:13], v213 offset:33792
	s_nop 0
	v_mfma_f32_32x32x16_bf16 v[34:49], v[2:5], v[6:9], 0
	ds_read_b128 v[6:9], v213 offset:9216
	s_waitcnt lgkmcnt(2)
	v_mul_f32_e32 v26, v16, v20
	v_mul_f32_e32 v27, v17, v21
	v_pk_mul_f32 v[50:51], v[14:15], v[18:19]
	s_mov_b32 s4, 0x3727c5ac
	s_waitcnt lgkmcnt(0)
	v_pk_mul_f32 v[8:9], v[8:9], v[24:25]
	v_pk_mul_f32 v[28:29], v[6:7], v[22:23]
	v_pk_fma_f32 v[90:91], v[16:17], v[20:21], v[8:9]
	v_pk_fma_f32 v[92:93], v[14:15], v[18:19], v[28:29]
	ds_read_b128 v[14:17], v213 offset:2048
	v_cvt_pk_bf16_f32 v9, v8, v9
	v_cvt_pk_bf16_f32 v7, v26, v27
	v_cvt_pk_bf16_f32 v8, v28, v29
	ds_read_b128 v[26:29], v213 offset:3072
	v_cvt_pk_bf16_f32 v6, v50, v51
	s_waitcnt lgkmcnt(1)
	v_pk_mul_f32 v[94:95], v[14:15], v[82:83]
	s_mov_b32 s0, 0x3c800000
	v_mfma_f32_32x32x16_bf16 v[50:65], v[2:5], v[6:9], 0
	v_mul_f32_e32 v2, v16, v84
	v_mul_f32_e32 v3, v17, v85
	s_waitcnt lgkmcnt(0)
	v_mul_f32_e32 v4, v28, v88
	v_mul_f32_e32 v5, v29, v89
	v_pk_mul_f32 v[6:7], v[26:27], v[86:87]
	v_pk_fma_f32 v[8:9], v[16:17], v[84:85], v[4:5]
	v_cvt_pk_bf16_f32 v3, v2, v3
	v_pk_fma_f32 v[14:15], v[14:15], v[82:83], v[6:7]
	v_pk_add_f32 v[26:27], v[8:9], v[30:31]
	v_cvt_pk_bf16_f32 v5, v4, v5
	v_cvt_pk_bf16_f32 v4, v6, v7
	ds_read_b128 v[6:9], v213 offset:10240
	v_pk_add_f32 v[28:29], v[14:15], v[32:33]
	ds_read_b128 v[14:17], v213 offset:11264
	v_cvt_pk_bf16_f32 v2, v94, v95
	s_waitcnt lgkmcnt(1)
	v_pk_mul_f32 v[30:31], v[6:7], v[82:83]
	v_mov_b64_e32 v[152:153], s[4:5]
	v_mfma_f32_32x32x16_bf16 v[34:49], v[10:13], v[2:5], v[34:49]
	v_mul_f32_e32 v2, v8, v84
	v_mul_f32_e32 v3, v9, v85
	s_waitcnt lgkmcnt(0)
	v_mul_f32_e32 v4, v16, v88
	v_mul_f32_e32 v5, v17, v89
	v_pk_mul_f32 v[14:15], v[14:15], v[86:87]
	v_pk_fma_f32 v[8:9], v[8:9], v[84:85], v[4:5]
	v_pk_fma_f32 v[6:7], v[6:7], v[82:83], v[14:15]
	v_cvt_pk_bf16_f32 v5, v4, v5
	v_cvt_pk_bf16_f32 v3, v2, v3
	v_cvt_pk_bf16_f32 v4, v14, v15
	v_pk_add_f32 v[32:33], v[8:9], v[90:91]
	v_pk_add_f32 v[90:91], v[6:7], v[92:93]
	ds_read_b128 v[6:9], v213 offset:34816
	ds_read_b128 v[14:17], v213 offset:4096
	v_cvt_pk_bf16_f32 v2, v30, v31
	s_mov_b32 s13, 0
	s_mov_b64 s[6:7], 0
	v_mfma_f32_32x32x16_bf16 v[50:65], v[10:13], v[2:5], v[50:65]
	ds_read_b128 v[2:5], v213 offset:5120
	ds_read_b128 v[10:13], v213 offset:12288
	s_waitcnt lgkmcnt(2)
	v_pk_mul_f32 v[30:31], v[16:17], v[76:77]
	v_pk_mul_f32 v[92:93], v[14:15], v[74:75]
	s_waitcnt lgkmcnt(1)
	v_pk_mul_f32 v[4:5], v[4:5], v[80:81]
	v_pk_mul_f32 v[94:95], v[2:3], v[78:79]
	v_pk_fma_f32 v[2:3], v[16:17], v[76:77], v[4:5]
	v_cvt_pk_bf16_f32 v5, v4, v5
	v_pk_add_f32 v[96:97], v[2:3], v[26:27]
	v_cvt_pk_bf16_f32 v3, v30, v31
	v_cvt_pk_bf16_f32 v4, v94, v95
	v_cvt_pk_bf16_f32 v2, v92, v93
	v_pk_fma_f32 v[14:15], v[14:15], v[74:75], v[94:95]
	s_waitcnt lgkmcnt(0)
	v_pk_mul_f32 v[30:31], v[10:11], v[74:75]
	v_mfma_f32_32x32x16_bf16 v[34:49], v[6:9], v[2:5], v[34:49]
	ds_read_b128 v[2:5], v213 offset:13312
	v_add_f32_e32 v98, v14, v28
	v_add_f32_e32 v99, v15, v29
	ds_read_b128 v[14:17], v213 offset:35840
	v_pk_mul_f32 v[26:27], v[12:13], v[76:77]
	s_waitcnt lgkmcnt(1)
	v_pk_mul_f32 v[4:5], v[4:5], v[80:81]
	v_pk_mul_f32 v[28:29], v[2:3], v[78:79]
	v_pk_fma_f32 v[2:3], v[12:13], v[76:77], v[4:5]
	v_pk_fma_f32 v[10:11], v[10:11], v[74:75], v[28:29]
	v_pk_add_f32 v[32:33], v[2:3], v[32:33]
	v_pk_add_f32 v[92:93], v[10:11], v[90:91]
	ds_read_b128 v[10:13], v213 offset:6144
	v_cvt_pk_bf16_f32 v5, v4, v5
	v_cvt_pk_bf16_f32 v3, v26, v27
	v_cvt_pk_bf16_f32 v4, v28, v29
	ds_read_b128 v[26:29], v213 offset:7168
	v_cvt_pk_bf16_f32 v2, v30, v31
	s_waitcnt lgkmcnt(1)
	v_pk_mul_f32 v[30:31], v[10:11], v[66:67]
	v_mfma_f32_32x32x16_bf16 v[50:65], v[6:9], v[2:5], v[50:65]
	v_mul_f32_e32 v2, v12, v68
	v_mul_f32_e32 v3, v13, v69
	s_waitcnt lgkmcnt(0)
	v_mul_f32_e32 v4, v28, v72
	v_mul_f32_e32 v5, v29, v73
	v_pk_mul_f32 v[6:7], v[26:27], v[70:71]
	v_pk_fma_f32 v[8:9], v[12:13], v[68:69], v[4:5]
	v_cvt_pk_bf16_f32 v3, v2, v3
	v_pk_fma_f32 v[10:11], v[10:11], v[66:67], v[6:7]
	v_pk_add_f32 v[94:95], v[8:9], v[96:97]
	v_cvt_pk_bf16_f32 v5, v4, v5
	v_cvt_pk_bf16_f32 v4, v6, v7
	ds_read_b128 v[6:9], v213 offset:14336
	v_pk_add_f32 v[96:97], v[10:11], v[98:99]
	ds_read_b128 v[10:13], v213 offset:15360
	v_cvt_pk_bf16_f32 v2, v30, v31
	s_waitcnt lgkmcnt(1)
	v_pk_mul_f32 v[30:31], v[6:7], v[66:67]
	v_mfma_f32_32x32x16_bf16 v[34:49], v[14:17], v[2:5], v[34:49]
	s_waitcnt lgkmcnt(0)
	v_mul_f32_e32 v10, v10, v70
	v_mul_f32_e32 v11, v11, v71
	v_mul_f32_e32 v2, v8, v68
	v_mul_f32_e32 v3, v9, v69
	v_pk_mul_f32 v[4:5], v[12:13], v[72:73]
	v_pk_fma_f32 v[6:7], v[6:7], v[66:67], v[10:11]
	v_pk_fma_f32 v[8:9], v[8:9], v[68:69], v[4:5]
	v_pk_add_f32 v[92:93], v[6:7], v[92:93]
	v_cvt_pk_bf16_f32 v3, v2, v3
	v_pk_add_f32 v[90:91], v[8:9], v[32:33]
	v_cvt_pk_bf16_f32 v5, v4, v5
	v_cvt_pk_bf16_f32 v4, v10, v11
	ds_read_b128 v[26:29], v213 offset:36864
	ds_read_b128 v[6:9], v213 offset:16384
	v_cvt_pk_bf16_f32 v2, v30, v31
	ds_read_b128 v[98:101], v213 offset:25600
	ds_read_b128 v[102:105], v213 offset:37888
	v_mfma_f32_32x32x16_bf16 v[50:65], v[14:17], v[2:5], v[50:65]
	ds_read_b128 v[2:5], v213 offset:17408
	ds_read_b128 v[30:33], v213 offset:24576
	s_waitcnt lgkmcnt(4)
	v_pk_mul_f32 v[12:13], v[6:7], v[18:19]
	v_pk_mul_f32 v[10:11], v[8:9], v[20:21]
	s_waitcnt lgkmcnt(1)
	v_pk_mul_f32 v[14:15], v[2:3], v[22:23]
	v_pk_mul_f32 v[22:23], v[98:99], v[22:23]
	v_pk_fma_f32 v[112:113], v[6:7], v[18:19], v[14:15]
	s_waitcnt lgkmcnt(0)
	v_pk_mul_f32 v[114:115], v[30:31], v[18:19]
	v_pk_fma_f32 v[118:119], v[30:31], v[18:19], v[22:23]
	v_pk_mul_f32 v[4:5], v[4:5], v[24:25]
	v_pk_mul_f32 v[106:107], v[32:33], v[20:21]
	v_pk_mul_f32 v[24:25], v[100:101], v[24:25]
	ds_read_b128 v[98:101], v213 offset:18432
	v_cvt_pk_bf16_f32 v19, v106, v107
	ds_read_b128 v[106:109], v213 offset:19456
	v_pk_fma_f32 v[110:111], v[8:9], v[20:21], v[4:5]
	v_cvt_pk_bf16_f32 v5, v4, v5
	v_cvt_pk_bf16_f32 v3, v10, v11
	v_cvt_pk_bf16_f32 v4, v14, v15
	s_waitcnt lgkmcnt(0)
	v_pk_mul_f32 v[106:107], v[106:107], v[86:87]
	v_cvt_pk_bf16_f32 v2, v12, v13
	v_pk_mul_f32 v[120:121], v[98:99], v[82:83]
	v_pk_mul_f32 v[108:109], v[108:109], v[88:89]
	v_pk_fma_f32 v[98:99], v[98:99], v[82:83], v[106:107]
	v_mfma_f32_32x32x16_bf16 v[2:17], v[26:29], v[2:5], 0
	v_cvt_pk_bf16_f32 v18, v114, v115
	v_mul_f32_e32 v114, v100, v84
	v_mul_f32_e32 v115, v101, v85
	v_fma_f32 v100, v100, v84, v108
	v_fma_f32 v101, v101, v85, v109
	v_pk_add_f32 v[124:125], v[98:99], v[112:113]
	v_pk_add_f32 v[122:123], v[100:101], v[110:111]
	v_cvt_pk_bf16_f32 v101, v108, v109
	v_cvt_pk_bf16_f32 v100, v106, v107
	ds_read_b128 v[106:109], v213 offset:26624
	v_pk_fma_f32 v[116:117], v[32:33], v[20:21], v[24:25]
	v_cvt_pk_bf16_f32 v21, v24, v25
	v_cvt_pk_bf16_f32 v20, v22, v23
	ds_read_b128 v[110:113], v213 offset:27648
	v_cvt_pk_bf16_f32 v99, v114, v115
	v_mfma_f32_32x32x16_bf16 v[18:33], v[26:29], v[18:21], 0
	v_cvt_pk_bf16_f32 v98, v120, v121
	s_waitcnt lgkmcnt(1)
	v_mul_f32_e32 v114, v106, v82
	v_mul_f32_e32 v115, v107, v83
	s_waitcnt lgkmcnt(0)
	v_pk_mul_f32 v[86:87], v[110:111], v[86:87]
	v_pk_mul_f32 v[88:89], v[112:113], v[88:89]
	v_pk_fma_f32 v[82:83], v[106:107], v[82:83], v[86:87]
	v_mfma_f32_32x32x16_bf16 v[2:17], v[102:105], v[98:101], v[2:17]
	v_mul_f32_e32 v98, v108, v84
	v_mul_f32_e32 v99, v109, v85
	v_fma_f32 v84, v108, v84, v88
	v_fma_f32 v85, v109, v85, v89
	v_add_f32_e32 v108, v82, v118
	v_add_f32_e32 v109, v83, v119
	v_cvt_pk_bf16_f32 v83, v98, v99
	v_pk_add_f32 v[106:107], v[84:85], v[116:117]
	v_cvt_pk_bf16_f32 v85, v88, v89
	v_cvt_pk_bf16_f32 v84, v86, v87
	ds_read_b128 v[86:89], v213 offset:38912
	ds_read_b128 v[98:101], v213 offset:20480
	v_cvt_pk_bf16_f32 v82, v114, v115
	s_waitcnt lgkmcnt(0)
	v_pk_mul_f32 v[110:111], v[100:101], v[76:77]
	v_mfma_f32_32x32x16_bf16 v[18:33], v[102:105], v[82:85], v[18:33]
	ds_read_b128 v[82:85], v213 offset:21504
	ds_read_b128 v[102:105], v213 offset:28672
	v_mul_f32_e32 v112, v98, v74
	v_mul_f32_e32 v113, v99, v75
	s_waitcnt lgkmcnt(1)
	v_pk_mul_f32 v[84:85], v[84:85], v[80:81]
	v_pk_mul_f32 v[114:115], v[82:83], v[78:79]
	v_pk_fma_f32 v[82:83], v[100:101], v[76:77], v[84:85]
	v_cvt_pk_bf16_f32 v85, v84, v85
	v_pk_add_f32 v[116:117], v[82:83], v[122:123]
	v_cvt_pk_bf16_f32 v83, v110, v111
	v_cvt_pk_bf16_f32 v84, v114, v115
	v_cvt_pk_bf16_f32 v82, v112, v113
	v_pk_fma_f32 v[98:99], v[98:99], v[74:75], v[114:115]
	s_waitcnt lgkmcnt(0)
	v_pk_mul_f32 v[112:113], v[102:103], v[74:75]
	v_mfma_f32_32x32x16_bf16 v[2:17], v[86:89], v[82:85], v[2:17]
	ds_read_b128 v[82:85], v213 offset:29696
	v_add_f32_e32 v118, v98, v124
	v_add_f32_e32 v119, v99, v125
	v_mul_f32_e32 v110, v104, v76
	v_mul_f32_e32 v111, v105, v77
	ds_read_b128 v[98:101], v213 offset:39936
	s_waitcnt lgkmcnt(1)
	v_pk_mul_f32 v[78:79], v[82:83], v[78:79]
	v_pk_mul_f32 v[80:81], v[84:85], v[80:81]
	v_pk_fma_f32 v[74:75], v[102:103], v[74:75], v[78:79]
	v_pk_fma_f32 v[76:77], v[104:105], v[76:77], v[80:81]
	v_pk_add_f32 v[104:105], v[74:75], v[108:109]
	v_pk_add_f32 v[102:103], v[76:77], v[106:107]
	v_cvt_pk_bf16_f32 v77, v80, v81
	v_cvt_pk_bf16_f32 v76, v78, v79
	ds_read_b128 v[78:81], v213 offset:22528
	ds_read_b128 v[82:85], v213 offset:23552
	v_cvt_pk_bf16_f32 v75, v110, v111
	v_cvt_pk_bf16_f32 v74, v112, v113
	s_waitcnt lgkmcnt(0)
	v_pk_mul_f32 v[82:83], v[82:83], v[70:71]
	v_mfma_f32_32x32x16_bf16 v[18:33], v[86:89], v[74:77], v[18:33]
	v_mul_f32_e32 v74, v80, v68
	v_mul_f32_e32 v75, v81, v69
	v_mul_f32_e32 v76, v84, v72
	v_mul_f32_e32 v77, v85, v73
	v_mul_f32_e32 v86, v78, v66
	v_mul_f32_e32 v87, v79, v67
	v_pk_fma_f32 v[80:81], v[80:81], v[68:69], v[76:77]
	v_pk_fma_f32 v[78:79], v[78:79], v[66:67], v[82:83]
	v_cvt_pk_bf16_f32 v75, v74, v75
	v_pk_add_f32 v[88:89], v[80:81], v[116:117]
	v_pk_add_f32 v[106:107], v[78:79], v[118:119]
	ds_read_b128 v[78:81], v213 offset:30720
	v_cvt_pk_bf16_f32 v77, v76, v77
	v_cvt_pk_bf16_f32 v76, v82, v83
	ds_read_b128 v[82:85], v213 offset:31744
	v_cvt_pk_bf16_f32 v74, v86, v87
	s_waitcnt lgkmcnt(0)
	v_pk_mul_f32 v[72:73], v[84:85], v[72:73]
	v_mfma_f32_32x32x16_bf16 v[2:17], v[98:101], v[74:77], v[2:17]
	v_mul_f32_e32 v74, v80, v68
	v_mul_f32_e32 v75, v81, v69
	v_fma_f32 v68, v80, v68, v72
	v_fma_f32 v69, v81, v69, v73
	v_mul_f32_e32 v70, v82, v70
	v_mul_f32_e32 v71, v83, v71
	v_pk_add_f32 v[84:85], v[68:69], v[102:103]
	v_cvt_pk_bf16_f32 v69, v72, v73
	v_add_f32_e32 v72, v97, v96
	v_add_f32_e32 v73, v94, v95
	v_pk_mul_f32 v[76:77], v[78:79], v[66:67]
	v_pk_fma_f32 v[66:67], v[78:79], v[66:67], v[70:71]
	v_add_f32_e32 v72, v72, v73
	v_pk_add_f32 v[86:87], v[66:67], v[104:105]
	v_mov_b32_e32 v66, v72
	s_nop 1
	v_permlane32_swap_b32_e32 v72, v66
	v_add_f32_e32 v66, v72, v66
	v_cvt_pk_bf16_f32 v67, v74, v75
	v_rcp_f32_e32 v74, v66
	v_cvt_pk_bf16_f32 v68, v70, v71
	v_cvt_pk_bf16_f32 v66, v76, v77
	v_pk_mul_f32 v[70:71], v[46:47], v[74:75] op_sel_hi:[1,0]
	s_nop 0
	v_mfma_f32_32x32x16_bf16 v[18:33], v[98:101], v[66:69], v[18:33]
	v_mul_f32_e32 v66, v42, v74
	v_mul_f32_e32 v67, v43, v74
	v_add_f32_e32 v42, v93, v92
	v_add_f32_e32 v43, v90, v91
	v_pk_mul_f32 v[68:69], v[44:45], v[74:75] op_sel_hi:[1,0]
	v_add_f32_e32 v42, v42, v43
	v_mov_b32_e32 v43, v42
	s_nop 1
	v_permlane32_swap_b32_e32 v42, v43
	v_add_f32_e32 v42, v42, v43
	v_rcp_f32_e32 v42, v42
	v_add_f32_e32 v44, v107, v106
	v_add_f32_e32 v45, v88, v89
	v_pk_mul_f32 v[72:73], v[48:49], v[74:75] op_sel_hi:[1,0]
	v_add_f32_e32 v44, v44, v45
	v_pk_mul_f32 v[36:37], v[36:37], v[74:75] op_sel_hi:[1,0]
	v_pk_mul_f32 v[38:39], v[38:39], v[74:75] op_sel_hi:[1,0]
	v_pk_mul_f32 v[40:41], v[40:41], v[74:75] op_sel_hi:[1,0]
	v_pk_mul_f32 v[34:35], v[34:35], v[74:75] op_sel_hi:[1,0]
	v_pk_mul_f32 v[74:75], v[58:59], v[42:43] op_sel_hi:[1,0]
	v_pk_mul_f32 v[78:79], v[60:61], v[42:43] op_sel_hi:[1,0]
	v_pk_mul_f32 v[80:81], v[62:63], v[42:43] op_sel_hi:[1,0]
	v_pk_mul_f32 v[82:83], v[64:65], v[42:43] op_sel_hi:[1,0]
	v_pk_mul_f32 v[92:93], v[52:53], v[42:43] op_sel_hi:[1,0]
	v_mov_b32_e32 v43, v44
	s_nop 1
	v_permlane32_swap_b32_e32 v44, v43
	v_add_f32_e32 v43, v44, v43
	v_rcp_f32_e32 v76, v43
	v_pk_mul_f32 v[96:97], v[54:55], v[42:43] op_sel_hi:[1,0]
	v_pk_mul_f32 v[94:95], v[56:57], v[42:43] op_sel_hi:[1,0]
	v_pk_mul_f32 v[98:99], v[50:51], v[42:43] op_sel_hi:[1,0]
	v_pk_mul_f32 v[100:101], v[4:5], v[76:77] op_sel_hi:[1,0]
	v_pk_mov_b32 v[4:5], v[86:87], v[84:85] op_sel:[1,0]
	v_mov_b32_e32 v87, v85
	v_pk_add_f32 v[4:5], v[4:5], v[86:87]
	v_pk_mul_f32 v[102:103], v[6:7], v[76:77] op_sel_hi:[1,0]
	v_pk_add_f32 v[104:105], v[4:5], v[4:5] op_sel:[0,1] op_sel_hi:[1,0]
	v_cvt_pk_bf16_f32 v7, v40, v41
	ds_read_b128 v[84:87], v150 offset:52224
	ds_read_b128 v[50:53], v150 offset:35840
	ds_read_b128 v[54:57], v150 offset:36864
	ds_read_b128 v[58:61], v150 offset:37888
	ds_read_b128 v[62:65], v150 offset:38912
	v_cvt_pk_bf16_f32 v6, v38, v39
	v_cvt_pk_bf16_f32 v5, v36, v37
	v_cvt_pk_bf16_f32 v4, v34, v35
	ds_read_b128 v[88:91], v150 offset:53248
	ds_read_b128 v[34:37], v150 offset:39936
	ds_read_b128 v[38:41], v150 offset:40960
	ds_read_b128 v[42:45], v150 offset:41984
	ds_read_b128 v[46:49], v150 offset:43008
	v_cvt_pk_bf16_f32 v95, v94, v95
	v_cvt_pk_bf16_f32 v94, v96, v97
	v_cvt_pk_bf16_f32 v93, v92, v93
	v_cvt_pk_bf16_f32 v92, v98, v99
	s_waitcnt lgkmcnt(5)
	v_mfma_f32_32x32x16_bf16 v[50:65], v[84:87], v[4:7], v[50:65]
	v_mul_f32_e32 v10, v10, v76
	v_mul_f32_e32 v11, v11, v76
	v_mul_f32_e32 v12, v12, v76
	v_mul_f32_e32 v13, v13, v76
	v_mul_f32_e32 v8, v8, v76
	v_mul_f32_e32 v9, v9, v76
	v_mov_b32_e32 v77, v104
	s_nop 1
	v_permlane32_swap_b32_e32 v104, v77
	v_cvt_pk_bf16_f32 v73, v72, v73
	s_waitcnt lgkmcnt(0)
	v_mfma_f32_32x32x16_bf16 v[34:49], v[84:87], v[92:95], v[34:49]
	v_cvt_pk_bf16_f32 v72, v70, v71
	v_cvt_pk_bf16_f32 v70, v66, v67
	v_add_f32_e32 v66, v104, v77
	v_cvt_pk_bf16_f32 v71, v68, v69
	v_rcp_f32_e32 v104, v66
	v_cvt_pk_bf16_f32 v69, v82, v83
	v_cvt_pk_bf16_f32 v68, v80, v81
	v_cvt_pk_bf16_f32 v67, v78, v79
	v_cvt_pk_bf16_f32 v66, v74, v75
	ds_read_b128 v[78:81], v150 offset:54272
	v_mfma_f32_32x32x16_bf16 v[50:65], v[88:91], v[70:73], v[50:65]
	v_mul_f32_e32 v2, v2, v76
	v_mul_f32_e32 v3, v3, v76
	v_mul_f32_e32 v20, v20, v104
	v_mul_f32_e32 v21, v21, v104
	v_cvt_pk_bf16_f32 v85, v8, v9
	v_cvt_pk_bf16_f32 v82, v2, v3
	v_pk_mul_f32 v[2:3], v[22:23], v[104:105] op_sel_hi:[1,0]
	v_pk_mul_f32 v[8:9], v[24:25], v[104:105] op_sel_hi:[1,0]
	v_pk_mul_f32 v[18:19], v[18:19], v[104:105] op_sel_hi:[1,0]
	v_mfma_f32_32x32x16_bf16 v[34:49], v[88:91], v[66:69], v[34:49]
	v_cvt_pk_bf16_f32 v84, v102, v103
	v_cvt_pk_bf16_f32 v83, v100, v101
	ds_read_b128 v[86:89], v150 offset:55296
	v_cvt_pk_bf16_f32 v99, v8, v9
	v_cvt_pk_bf16_f32 v98, v2, v3
	v_cvt_pk_bf16_f32 v97, v20, v21
	v_cvt_pk_bf16_f32 v96, v18, v19
	s_waitcnt lgkmcnt(1)
	v_mfma_f32_32x32x16_bf16 v[50:65], v[78:81], v[82:85], v[50:65]
	v_mul_f32_e32 v2, v14, v76
	v_mul_f32_e32 v3, v15, v76
	v_mul_f32_e32 v8, v16, v76
	v_mul_f32_e32 v9, v17, v76
	v_mul_f32_e32 v14, v26, v104
	v_mul_f32_e32 v15, v27, v104
	v_cvt_pk_bf16_f32 v77, v8, v9
	v_cvt_pk_bf16_f32 v76, v2, v3
	v_cvt_pk_bf16_f32 v74, v10, v11
	v_pk_mul_f32 v[2:3], v[28:29], v[104:105] op_sel_hi:[1,0]
	v_mfma_f32_32x32x16_bf16 v[34:49], v[78:81], v[96:99], v[34:49]
	v_mul_f32_e32 v8, v30, v104
	v_mul_f32_e32 v9, v31, v104
	v_mul_f32_e32 v10, v32, v104
	v_mul_f32_e32 v11, v33, v104
	v_cvt_pk_bf16_f32 v75, v12, v13
	v_cvt_pk_bf16_f32 v81, v10, v11
	v_cvt_pk_bf16_f32 v80, v8, v9
	v_cvt_pk_bf16_f32 v79, v2, v3
	v_cvt_pk_bf16_f32 v78, v14, v15
	s_waitcnt lgkmcnt(0)
	v_mfma_f32_32x32x16_bf16 v[50:65], v[86:89], v[74:77], v[50:65]
	v_mfma_f32_32x32x16_bf16 v[34:49], v[86:89], v[78:81], v[34:49]
	ds_read_b128 v[86:89], v150 offset:56320
	ds_read_b128 v[18:21], v150 offset:44032
	ds_read_b128 v[22:25], v150 offset:45056
	ds_read_b128 v[26:29], v150 offset:46080
	ds_read_b128 v[30:33], v150 offset:47104
	ds_read_b128 v[100:103], v150 offset:57344
	s_waitcnt lgkmcnt(1)
	v_mfma_f32_32x32x16_bf16 v[18:33], v[86:89], v[4:7], v[18:33]
	ds_read_b128 v[2:5], v150 offset:48128
	ds_read_b128 v[6:9], v150 offset:49152
	ds_read_b128 v[10:13], v150 offset:50176
	ds_read_b128 v[14:17], v150 offset:51200
	s_waitcnt lgkmcnt(0)
	v_mfma_f32_32x32x16_bf16 v[2:17], v[86:89], v[92:95], v[2:17]
	v_mfma_f32_32x32x16_bf16 v[18:33], v[100:103], v[70:73], v[18:33]
	v_mfma_f32_32x32x16_bf16 v[2:17], v[100:103], v[66:69], v[2:17]
	ds_read_b128 v[66:69], v150 offset:58368
	ds_read_b128 v[70:73], v150 offset:59392
	s_waitcnt lgkmcnt(1)
	v_mfma_f32_32x32x16_bf16 v[18:33], v[66:69], v[82:85], v[18:33]
	v_mfma_f32_32x32x16_bf16 v[2:17], v[66:69], v[96:99], v[2:17]
	s_waitcnt lgkmcnt(0)
	v_mfma_f32_32x32x16_bf16 v[18:33], v[70:73], v[74:77], v[18:33]
	v_mfma_f32_32x32x16_bf16 v[2:17], v[70:73], v[78:81], v[2:17]
	s_nop 10
	v_mul_f32_e32 v66, v22, v22
	v_mul_f32_e32 v67, v23, v23
	v_mul_f32_e32 v68, v30, v30
	v_mul_f32_e32 v69, v31, v31
	v_mul_f32_e32 v70, v24, v24
	v_mul_f32_e32 v71, v25, v25
	v_pk_mul_f32 v[72:73], v[32:33], v[32:33]
	v_pk_mul_f32 v[74:75], v[20:21], v[20:21]
	v_pk_mul_f32 v[76:77], v[28:29], v[28:29]
	v_pk_mul_f32 v[78:79], v[26:27], v[26:27]
	v_pk_mul_f32 v[80:81], v[18:19], v[18:19]
	v_pk_fma_f32 v[78:79], v[58:59], v[58:59], v[78:79]
	v_pk_fma_f32 v[76:77], v[60:61], v[60:61], v[76:77]
	v_pk_fma_f32 v[74:75], v[52:53], v[52:53], v[74:75]
	v_pk_fma_f32 v[72:73], v[64:65], v[64:65], v[72:73]
	v_pk_fma_f32 v[70:71], v[56:57], v[56:57], v[70:71]
	v_pk_fma_f32 v[68:69], v[62:63], v[62:63], v[68:69]
	v_pk_fma_f32 v[66:67], v[54:55], v[54:55], v[66:67]
	v_pk_fma_f32 v[80:81], v[50:51], v[50:51], v[80:81]
	v_pk_add_f32 v[66:67], v[66:67], v[68:69]
	v_pk_add_f32 v[68:69], v[70:71], v[72:73]
	v_pk_add_f32 v[70:71], v[74:75], v[76:77]
	v_pk_add_f32 v[72:73], v[80:81], v[78:79]
	v_pk_add_f32 v[68:69], v[70:71], v[68:69]
	v_pk_add_f32 v[66:67], v[72:73], v[66:67]
	v_pk_mul_f32 v[72:73], v[14:15], v[14:15]
	v_pk_mov_b32 v[70:71], v[66:67], v[68:69] op_sel:[1,0]
	v_mov_b32_e32 v67, v69
	v_pk_add_f32 v[66:67], v[70:71], v[66:67]
	v_pk_mul_f32 v[70:71], v[6:7], v[6:7]
	v_pk_mul_f32 v[74:75], v[8:9], v[8:9]
	v_pk_mul_f32 v[76:77], v[16:17], v[16:17]
	v_pk_mul_f32 v[78:79], v[4:5], v[4:5]
	v_pk_mul_f32 v[80:81], v[12:13], v[12:13]
	v_pk_mul_f32 v[82:83], v[10:11], v[10:11]
	v_pk_mul_f32 v[84:85], v[2:3], v[2:3]
	v_pk_fma_f32 v[82:83], v[42:43], v[42:43], v[82:83]
	v_pk_fma_f32 v[80:81], v[44:45], v[44:45], v[80:81]
	v_pk_fma_f32 v[78:79], v[36:37], v[36:37], v[78:79]
	v_pk_fma_f32 v[76:77], v[48:49], v[48:49], v[76:77]
	v_pk_fma_f32 v[74:75], v[40:41], v[40:41], v[74:75]
	v_pk_fma_f32 v[72:73], v[46:47], v[46:47], v[72:73]
	v_pk_fma_f32 v[70:71], v[38:39], v[38:39], v[70:71]
	v_pk_fma_f32 v[84:85], v[34:35], v[34:35], v[84:85]
	v_pk_add_f32 v[70:71], v[70:71], v[72:73]
	v_pk_add_f32 v[72:73], v[74:75], v[76:77]
	v_pk_add_f32 v[74:75], v[78:79], v[80:81]
	v_pk_add_f32 v[76:77], v[84:85], v[82:83]
	v_pk_add_f32 v[72:73], v[74:75], v[72:73]
	v_pk_add_f32 v[70:71], v[76:77], v[70:71]
	v_pk_add_f32 v[66:67], v[66:67], v[66:67] op_sel:[0,1] op_sel_hi:[1,0]
	v_add_f32_e32 v70, v71, v70
	v_add_f32_e32 v71, v72, v73
	v_mov_b32_e32 v69, v66
	v_add_f32_e32 v70, v70, v71
	s_nop 0
	v_permlane32_swap_b32_e32 v66, v69
	v_mov_b32_e32 v68, v70
	s_nop 1
	v_permlane32_swap_b32_e32 v70, v68
	v_mov_b32_e32 v71, v66
	v_pk_add_f32 v[66:67], v[70:71], v[68:69]
	v_pk_fma_f32 v[66:67], v[66:67], s[0:1], v[152:153] op_sel_hi:[1,0,0]
	s_mov_b32 s1, 0x800000
	v_rsq_f32_e32 v68, v67
	s_nop 0
	v_pk_mul_f32 v[158:159], v[50:51], v[68:69] op_sel_hi:[1,0]
	v_pk_mul_f32 v[50:51], v[18:19], v[68:69] op_sel_hi:[1,0]
	v_pk_mul_f32 v[80:81], v[60:61], v[68:69] op_sel_hi:[1,0]
	v_pk_mul_f32 v[60:61], v[28:29], v[68:69] op_sel_hi:[1,0]
	v_pk_mul_f32 v[78:79], v[58:59], v[68:69] op_sel_hi:[1,0]
	v_pk_mul_f32 v[160:161], v[52:53], v[68:69] op_sel_hi:[1,0]
	v_pk_mul_f32 v[82:83], v[54:55], v[68:69] op_sel_hi:[1,0]
	v_rsq_f32_e32 v28, v66
	v_pk_mul_f32 v[168:169], v[56:57], v[68:69] op_sel_hi:[1,0]
	v_pk_mul_f32 v[58:59], v[26:27], v[68:69] op_sel_hi:[1,0]
	v_pk_mul_f32 v[52:53], v[20:21], v[68:69] op_sel_hi:[1,0]
	v_pk_mul_f32 v[54:55], v[22:23], v[68:69] op_sel_hi:[1,0]
	v_pk_mul_f32 v[56:57], v[24:25], v[68:69] op_sel_hi:[1,0]
	v_pk_mul_f32 v[18:19], v[42:43], v[28:29] op_sel_hi:[1,0]
	v_pk_mul_f32 v[20:21], v[44:45], v[28:29] op_sel_hi:[1,0]
	v_pk_mul_f32 v[22:23], v[46:47], v[28:29] op_sel_hi:[1,0]
	v_pk_mul_f32 v[26:27], v[48:49], v[28:29] op_sel_hi:[1,0]
	v_pk_mul_f32 v[162:163], v[34:35], v[28:29] op_sel_hi:[1,0]
	v_pk_mul_f32 v[164:165], v[36:37], v[28:29] op_sel_hi:[1,0]
	v_pk_mul_f32 v[166:167], v[38:39], v[28:29] op_sel_hi:[1,0]
	v_pk_mul_f32 v[24:25], v[40:41], v[28:29] op_sel_hi:[1,0]
	v_pk_mul_f32 v[104:105], v[2:3], v[28:29] op_sel_hi:[1,0]
	v_pk_mul_f32 v[112:113], v[4:5], v[28:29] op_sel_hi:[1,0]
	ds_read_b128 v[2:5], v150 offset:60416
	ds_read_b128 v[34:37], v174 offset:32768
	ds_read_b128 v[38:41], v174 offset:32800
	ds_read_b128 v[42:45], v174 offset:32832
	ds_read_b128 v[46:49], v174 offset:32864
	v_cvt_pk_bf16_f32 v129, v168, v169
	v_cvt_pk_bf16_f32 v128, v82, v83
	v_cvt_pk_bf16_f32 v127, v160, v161
	v_cvt_pk_bf16_f32 v126, v158, v159
	v_cvt_pk_bf16_f32 v137, v24, v25
	v_cvt_pk_bf16_f32 v136, v166, v167
	v_cvt_pk_bf16_f32 v135, v164, v165
	s_waitcnt lgkmcnt(0)
	v_mfma_f32_32x32x16_bf16 v[86:101], v[2:5], v[126:129], v[34:49]
	v_cvt_pk_bf16_f32 v134, v162, v163
	v_mul_f32_e32 v84, v62, v68
	v_mul_f32_e32 v85, v63, v68
	v_mul_f32_e32 v170, v64, v68
	v_mul_f32_e32 v171, v65, v68
	v_pk_mul_f32 v[62:63], v[30:31], v[68:69] op_sel_hi:[1,0]
	v_pk_mul_f32 v[64:65], v[32:33], v[68:69] op_sel_hi:[1,0]
	v_pk_mul_f32 v[116:117], v[6:7], v[28:29] op_sel_hi:[1,0]
	v_pk_mul_f32 v[154:155], v[8:9], v[28:29] op_sel_hi:[1,0]
	v_mfma_f32_32x32x16_bf16 v[34:49], v[2:5], v[134:137], v[34:49]
	ds_read_b128 v[6:9], v150 offset:61440
	ds_read_b128 v[66:69], v174 offset:32896
	ds_read_b128 v[106:109], v150 offset:64512
	v_cvt_pk_bf16_f32 v125, v170, v171
	v_cvt_pk_bf16_f32 v124, v84, v85
	v_cvt_pk_bf16_f32 v123, v80, v81
	v_cvt_pk_bf16_f32 v122, v78, v79
	v_cvt_pk_bf16_f32 v149, v26, v27
	v_cvt_pk_bf16_f32 v148, v22, v23
	v_cvt_pk_bf16_f32 v147, v20, v21
	v_cvt_pk_bf16_f32 v146, v18, v19
	s_waitcnt lgkmcnt(2)
	v_mfma_f32_32x32x16_bf16 v[86:101], v[6:9], v[122:125], v[86:101]
	v_mul_f32_e32 v102, v10, v28
	v_mul_f32_e32 v103, v11, v28
	v_mul_f32_e32 v110, v12, v28
	v_mul_f32_e32 v111, v13, v28
	v_mul_f32_e32 v114, v14, v28
	v_mul_f32_e32 v115, v15, v28
	v_pk_mul_f32 v[156:157], v[16:17], v[28:29] op_sel_hi:[1,0]
	ds_read_b128 v[176:179], v174 offset:33536
	ds_read_b128 v[180:183], v174 offset:33568
	ds_read_b128 v[184:187], v174 offset:33600
	ds_read_b128 v[28:31], v174 offset:33632
	ds_read_b128 v[188:191], v174 offset:33792
	ds_read_b128 v[192:195], v174 offset:33824
	ds_read_b128 v[196:199], v174 offset:33856
	ds_read_b128 v[200:203], v174 offset:33888
	ds_read_b128 v[204:207], v150 offset:62464
	v_cvt_pk_bf16_f32 v133, v56, v57
	v_mfma_f32_32x32x16_bf16 v[34:49], v[6:9], v[146:149], v[34:49]
	v_cvt_pk_bf16_f32 v132, v54, v55
	v_cvt_pk_bf16_f32 v131, v52, v53
	v_cvt_pk_bf16_f32 v130, v50, v51
	ds_read_b128 v[70:73], v174 offset:33664
	ds_read_b128 v[74:77], v174 offset:33920
	ds_read_b128 v[208:211], v150 offset:63488
	v_cvt_pk_bf16_f32 v145, v154, v155
	v_cvt_pk_bf16_f32 v144, v116, v117
	v_cvt_pk_bf16_f32 v143, v112, v113
	v_cvt_pk_bf16_f32 v142, v104, v105
	s_waitcnt lgkmcnt(3)
	v_mfma_f32_32x32x16_bf16 v[86:101], v[204:207], v[130:133], v[86:101]
	v_cvt_pk_bf16_f32 v121, v64, v65
	v_cvt_pk_bf16_f32 v120, v62, v63
	v_cvt_pk_bf16_f32 v119, v60, v61
	v_cvt_pk_bf16_f32 v118, v58, v59
	v_cvt_pk_bf16_f32 v141, v156, v157
	v_cvt_pk_bf16_f32 v140, v114, v115
	v_cvt_pk_bf16_f32 v139, v110, v111
	v_mfma_f32_32x32x16_bf16 v[34:49], v[204:207], v[142:145], v[34:49]
	v_cvt_pk_bf16_f32 v138, v102, v103
	v_fma_f32 v16, v30, v170, v202
	v_fma_f32 v17, v31, v171, v203
	v_fma_f32 v14, v28, v84, v200
	v_fma_f32 v15, v29, v85, v201
	v_pk_fma_f32 v[12:13], v[186:187], v[80:81], v[198:199]
	v_pk_fma_f32 v[10:11], v[184:185], v[78:79], v[196:197]
	v_pk_fma_f32 v[8:9], v[182:183], v[168:169], v[194:195]
	s_waitcnt lgkmcnt(0)
	v_mfma_f32_32x32x16_bf16 v[86:101], v[208:211], v[118:121], v[86:101]
	v_fma_f32 v6, v180, v82, v192
	v_fma_f32 v7, v181, v83, v193
	ds_read_b128 v[78:81], v174 offset:33760
	ds_read_b128 v[82:85], v174 offset:33248
	v_fma_f32 v4, v178, v160, v190
	v_fma_f32 v5, v179, v161, v191
	v_pk_fma_f32 v[2:3], v[176:177], v[158:159], v[188:189]
	v_pk_fma_f32 v[32:33], v[30:31], v[26:27], v[202:203]
	v_pk_fma_f32 v[30:31], v[28:29], v[22:23], v[200:201]
	v_pk_fma_f32 v[28:29], v[186:187], v[20:21], v[198:199]
	v_pk_fma_f32 v[26:27], v[184:185], v[18:19], v[196:197]
	v_pk_fma_f32 v[24:25], v[182:183], v[24:25], v[194:195]
	v_pk_fma_f32 v[22:23], v[180:181], v[166:167], v[192:193]
	v_pk_fma_f32 v[20:21], v[178:179], v[164:165], v[190:191]
	v_pk_fma_f32 v[18:19], v[176:177], v[162:163], v[188:189]
	ds_read_b128 v[158:161], v174 offset:33696
	ds_read_b128 v[162:165], v174 offset:33728
	ds_read_b128 v[166:169], v174 offset:33952
	ds_read_b128 v[176:179], v174 offset:33984
	ds_read_b128 v[180:183], v174 offset:34016
	ds_read_b128 v[184:187], v212 offset:11264
	v_mfma_f32_32x32x16_bf16 v[34:49], v[208:211], v[138:141], v[34:49]
	v_cvt_pk_bf16_f32 v86, v86, v87
	v_cvt_pk_bf16_f32 v87, v88, v89
	v_cvt_pk_bf16_f32 v88, v90, v91
	v_cvt_pk_bf16_f32 v89, v92, v93
	ds_read_b128 v[90:93], v212 offset:12288
	v_pk_max_i16 v86, v86, 0
	v_pk_max_i16 v87, v87, 0
	v_pk_max_i16 v88, v88, 0
	v_pk_max_i16 v89, v89, 0
	s_nop 1
	s_nop 0
	v_cvt_pk_bf16_f32 v188, v34, v35
	v_cvt_pk_bf16_f32 v189, v36, v37
	v_cvt_pk_bf16_f32 v190, v38, v39
	v_cvt_pk_bf16_f32 v191, v40, v41
	s_waitcnt lgkmcnt(1)
	v_mfma_f32_32x32x16_bf16 v[2:17], v[184:187], v[86:89], v[2:17]
	v_pk_max_i16 v188, v188, 0
	v_pk_max_i16 v189, v189, 0
	v_pk_max_i16 v190, v190, 0
	v_pk_max_i16 v191, v191, 0
	v_cvt_pk_bf16_f32 v94, v94, v95
	v_cvt_pk_bf16_f32 v95, v96, v97
	v_cvt_pk_bf16_f32 v96, v98, v99
	v_cvt_pk_bf16_f32 v97, v100, v101
	v_cvt_pk_bf16_f32 v98, v42, v43
	v_cvt_pk_bf16_f32 v99, v44, v45
	v_mfma_f32_32x32x16_bf16 v[18:33], v[184:187], v[188:191], v[18:33]
	ds_read_b128 v[184:187], v212 offset:19456
	v_cvt_pk_bf16_f32 v100, v46, v47
	v_cvt_pk_bf16_f32 v101, v48, v49
	v_fma_f32 v64, v80, v64, v182
	v_fma_f32 v65, v81, v65, v183
	v_pk_fma_f32 v[62:63], v[78:79], v[62:63], v[180:181]
	v_pk_fma_f32 v[60:61], v[164:165], v[60:61], v[178:179]
	v_pk_fma_f32 v[58:59], v[162:163], v[58:59], v[176:177]
	v_pk_max_i16 v94, v94, 0
	v_pk_max_i16 v95, v95, 0
	v_pk_max_i16 v96, v96, 0
	v_pk_max_i16 v97, v97, 0
	v_pk_max_i16 v98, v98, 0
	v_pk_max_i16 v99, v99, 0
	v_pk_max_i16 v100, v100, 0
	v_pk_max_i16 v101, v101, 0
	v_pk_fma_f32 v[56:57], v[160:161], v[56:57], v[168:169]
	s_waitcnt lgkmcnt(1)
	v_mfma_f32_32x32x16_bf16 v[2:17], v[90:93], v[94:97], v[2:17]
	v_fma_f32 v54, v158, v54, v166
	v_fma_f32 v55, v159, v55, v167
	v_fma_f32 v52, v72, v52, v76
	v_fma_f32 v53, v73, v53, v77
	v_fma_f32 v50, v70, v50, v74
	v_fma_f32 v51, v71, v51, v75
	v_pk_fma_f32 v[48:49], v[80:81], v[156:157], v[182:183]
	v_pk_fma_f32 v[46:47], v[78:79], v[114:115], v[180:181]
	v_pk_fma_f32 v[44:45], v[164:165], v[110:111], v[178:179]
	v_pk_fma_f32 v[42:43], v[162:163], v[102:103], v[176:177]
	v_mfma_f32_32x32x16_bf16 v[18:33], v[90:93], v[98:101], v[18:33]
	ds_read_b128 v[90:93], v212 offset:20480
	v_fma_f32 v40, v160, v154, v168
	v_fma_f32 v41, v161, v155, v169
	v_fma_f32 v38, v158, v116, v166
	v_fma_f32 v39, v159, v117, v167
	v_pk_fma_f32 v[36:37], v[72:73], v[112:113], v[76:77]
	v_pk_fma_f32 v[34:35], v[70:71], v[104:105], v[74:75]
	s_waitcnt lgkmcnt(1)
	v_mfma_f32_32x32x16_bf16 v[50:65], v[184:187], v[86:89], v[50:65]
	ds_read_b128 v[70:73], v174 offset:32928
	ds_read_b128 v[74:77], v174 offset:32960
	ds_read_b128 v[78:81], v174 offset:32992
	ds_read_b128 v[86:89], v174 offset:33024
	ds_read_b128 v[110:113], v212 offset:1024
	v_mfma_f32_32x32x16_bf16 v[34:49], v[184:187], v[188:191], v[34:49]
	s_waitcnt lgkmcnt(5)
	v_mfma_f32_32x32x16_bf16 v[50:65], v[90:93], v[94:97], v[50:65]
	v_mfma_f32_32x32x16_bf16 v[34:49], v[90:93], v[98:101], v[34:49]
	s_waitcnt lgkmcnt(2)
	v_mfma_f32_32x32x16_bf16 v[90:105], v[106:109], v[126:129], v[66:81]
	v_mfma_f32_32x32x16_bf16 v[66:81], v[106:109], v[134:137], v[66:81]
	ds_read_b128 v[106:109], v212 offset:0
	s_waitcnt lgkmcnt(0)
	v_mfma_f32_32x32x16_bf16 v[90:105], v[106:109], v[122:125], v[90:105]
	v_mfma_f32_32x32x16_bf16 v[66:81], v[106:109], v[146:149], v[66:81]
	ds_read_b128 v[106:109], v212 offset:2048
	v_mfma_f32_32x32x16_bf16 v[90:105], v[110:113], v[130:133], v[90:105]
	v_mfma_f32_32x32x16_bf16 v[66:81], v[110:113], v[142:145], v[66:81]
	ds_read_b128 v[110:113], v212 offset:13312
	s_waitcnt lgkmcnt(1)
	v_mfma_f32_32x32x16_bf16 v[90:105], v[106:109], v[118:121], v[90:105]
	v_mfma_f32_32x32x16_bf16 v[66:81], v[106:109], v[138:141], v[66:81]
	s_nop 10
	v_cvt_pk_bf16_f32 v90, v90, v91
	v_cvt_pk_bf16_f32 v91, v92, v93
	v_cvt_pk_bf16_f32 v92, v94, v95
	v_cvt_pk_bf16_f32 v94, v98, v99
	v_cvt_pk_bf16_f32 v95, v100, v101
	ds_read_b128 v[98:101], v212 offset:21504
	v_cvt_pk_bf16_f32 v66, v66, v67
	v_cvt_pk_bf16_f32 v67, v68, v69
	v_cvt_pk_bf16_f32 v68, v70, v71
	v_cvt_pk_bf16_f32 v93, v96, v97
	v_cvt_pk_bf16_f32 v69, v72, v73
	ds_read_b128 v[70:73], v212 offset:14336
	v_pk_max_i16 v90, v90, 0
	v_pk_max_i16 v91, v91, 0
	v_pk_max_i16 v92, v92, 0
	v_pk_max_i16 v93, v93, 0
	v_pk_max_i16 v66, v66, 0
	v_pk_max_i16 v67, v67, 0
	v_pk_max_i16 v68, v68, 0
	v_pk_max_i16 v69, v69, 0
	v_cvt_pk_bf16_f32 v96, v102, v103
	s_waitcnt lgkmcnt(2)
	v_mfma_f32_32x32x16_bf16 v[2:17], v[110:113], v[90:93], v[2:17]
	v_cvt_pk_bf16_f32 v97, v104, v105
	v_cvt_pk_bf16_f32 v74, v74, v75
	v_cvt_pk_bf16_f32 v75, v76, v77
	v_cvt_pk_bf16_f32 v76, v78, v79
	v_cvt_pk_bf16_f32 v77, v80, v81
	v_pk_max_i16 v94, v94, 0
	v_pk_max_i16 v95, v95, 0
	v_pk_max_i16 v96, v96, 0
	v_pk_max_i16 v97, v97, 0
	v_pk_max_i16 v74, v74, 0
	v_pk_max_i16 v75, v75, 0
	v_pk_max_i16 v76, v76, 0
	v_pk_max_i16 v77, v77, 0
	v_mfma_f32_32x32x16_bf16 v[18:33], v[110:113], v[66:69], v[18:33]
	s_waitcnt lgkmcnt(1)
	v_mfma_f32_32x32x16_bf16 v[34:49], v[98:101], v[66:69], v[34:49]
	ds_read_b128 v[66:69], v212 offset:22528
	v_mfma_f32_32x32x16_bf16 v[50:65], v[98:101], v[90:93], v[50:65]
	s_waitcnt lgkmcnt(1)
	v_mfma_f32_32x32x16_bf16 v[2:17], v[70:73], v[94:97], v[2:17]
	v_mfma_f32_32x32x16_bf16 v[18:33], v[70:73], v[74:77], v[18:33]
	ds_read_b128 v[78:81], v212 offset:3072
	s_waitcnt lgkmcnt(1)
	v_mfma_f32_32x32x16_bf16 v[50:65], v[66:69], v[94:97], v[50:65]
	ds_read_b128 v[90:93], v174 offset:33056
	ds_read_b128 v[94:97], v174 offset:33088
	ds_read_b128 v[98:101], v174 offset:33120
	ds_read_b128 v[70:73], v174 offset:33152
	v_mfma_f32_32x32x16_bf16 v[34:49], v[66:69], v[74:77], v[34:49]
	ds_read_b128 v[66:69], v212 offset:4096
	ds_read_b128 v[74:77], v212 offset:5120
	s_waitcnt lgkmcnt(3)
	v_mfma_f32_32x32x16_bf16 v[102:117], v[78:81], v[126:129], v[86:101]
	v_mfma_f32_32x32x16_bf16 v[86:101], v[78:81], v[134:137], v[86:101]
	s_waitcnt lgkmcnt(1)
	v_mfma_f32_32x32x16_bf16 v[86:101], v[66:69], v[146:149], v[86:101]
	v_mfma_f32_32x32x16_bf16 v[102:117], v[66:69], v[122:125], v[102:117]
	ds_read_b128 v[66:69], v212 offset:6144
	s_waitcnt lgkmcnt(1)
	v_mfma_f32_32x32x16_bf16 v[86:101], v[74:77], v[142:145], v[86:101]
	v_mfma_f32_32x32x16_bf16 v[102:117], v[74:77], v[130:133], v[102:117]
	ds_read_b128 v[74:77], v212 offset:15360
	s_waitcnt lgkmcnt(1)
	v_mfma_f32_32x32x16_bf16 v[86:101], v[66:69], v[138:141], v[86:101]
	v_mfma_f32_32x32x16_bf16 v[102:117], v[66:69], v[118:121], v[102:117]
	s_nop 10
	v_cvt_pk_bf16_f32 v78, v86, v87
	v_cvt_pk_bf16_f32 v80, v90, v91
	v_cvt_pk_bf16_f32 v79, v88, v89
	v_cvt_pk_bf16_f32 v81, v92, v93
	ds_read_b128 v[86:89], v212 offset:16384
	ds_read_b128 v[90:93], v212 offset:23552
	v_cvt_pk_bf16_f32 v66, v102, v103
	v_cvt_pk_bf16_f32 v67, v104, v105
	v_cvt_pk_bf16_f32 v68, v106, v107
	v_cvt_pk_bf16_f32 v69, v108, v109
	v_pk_max_i16 v66, v66, 0
	v_pk_max_i16 v67, v67, 0
	v_pk_max_i16 v68, v68, 0
	v_pk_max_i16 v69, v69, 0
	v_pk_max_i16 v78, v78, 0
	v_pk_max_i16 v79, v79, 0
	v_pk_max_i16 v80, v80, 0
	v_pk_max_i16 v81, v81, 0
	v_cvt_pk_bf16_f32 v94, v94, v95
	s_waitcnt lgkmcnt(2)
	v_mfma_f32_32x32x16_bf16 v[18:33], v[74:77], v[78:81], v[18:33]
	v_cvt_pk_bf16_f32 v95, v96, v97
	v_cvt_pk_bf16_f32 v96, v98, v99
	v_cvt_pk_bf16_f32 v97, v100, v101
	v_pk_max_i16 v94, v94, 0
	v_pk_max_i16 v95, v95, 0
	v_pk_max_i16 v96, v96, 0
	v_pk_max_i16 v97, v97, 0
	v_mfma_f32_32x32x16_bf16 v[2:17], v[74:77], v[66:69], v[2:17]
	v_cvt_pk_bf16_f32 v74, v110, v111
	v_cvt_pk_bf16_f32 v75, v112, v113
	v_cvt_pk_bf16_f32 v76, v114, v115
	v_cvt_pk_bf16_f32 v77, v116, v117
	v_pk_max_i16 v74, v74, 0
	v_pk_max_i16 v75, v75, 0
	v_pk_max_i16 v76, v76, 0
	v_pk_max_i16 v77, v77, 0
	s_waitcnt lgkmcnt(0)
	v_mfma_f32_32x32x16_bf16 v[50:65], v[90:93], v[66:69], v[50:65]
	ds_read_b128 v[66:69], v212 offset:24576
	v_mfma_f32_32x32x16_bf16 v[34:49], v[90:93], v[78:81], v[34:49]
	ds_read_b128 v[102:105], v212 offset:7168
	v_mfma_f32_32x32x16_bf16 v[2:17], v[86:89], v[74:77], v[2:17]
	s_waitcnt lgkmcnt(1)
	v_mfma_f32_32x32x16_bf16 v[50:65], v[66:69], v[74:77], v[50:65]
	ds_read_b128 v[74:77], v174 offset:33184
	ds_read_b128 v[78:81], v174 offset:33216
	v_mfma_f32_32x32x16_bf16 v[34:49], v[66:69], v[94:97], v[34:49]
	ds_read_b128 v[66:69], v212 offset:8192
	v_mfma_f32_32x32x16_bf16 v[18:33], v[86:89], v[94:97], v[18:33]
	s_waitcnt lgkmcnt(1)
	v_mfma_f32_32x32x16_bf16 v[86:101], v[102:105], v[126:129], v[70:85]
	v_mfma_f32_32x32x16_bf16 v[70:85], v[102:105], v[134:137], v[70:85]
	ds_read_b128 v[102:105], v212 offset:9216
	v_lshlrev_b32_e32 v135, 2, v1
	v_add_u32_e32 v134, v172, v174
	s_waitcnt lgkmcnt(1)
	v_mfma_f32_32x32x16_bf16 v[86:101], v[66:69], v[122:125], v[86:101]
	v_mfma_f32_32x32x16_bf16 v[70:85], v[66:69], v[146:149], v[70:85]
	ds_read_b128 v[66:69], v212 offset:10240
	s_waitcnt lgkmcnt(1)
	v_mfma_f32_32x32x16_bf16 v[86:101], v[102:105], v[130:133], v[86:101]
	v_mfma_f32_32x32x16_bf16 v[70:85], v[102:105], v[142:145], v[70:85]
	ds_read_b128 v[102:105], v212 offset:17408
	s_waitcnt lgkmcnt(1)
	v_mfma_f32_32x32x16_bf16 v[86:101], v[66:69], v[118:121], v[86:101]
	v_mfma_f32_32x32x16_bf16 v[70:85], v[66:69], v[138:141], v[70:85]
	s_nop 10
	v_cvt_pk_bf16_f32 v68, v90, v91
	v_cvt_pk_bf16_f32 v69, v92, v93
	ds_read_b128 v[90:93], v212 offset:25600
	v_cvt_pk_bf16_f32 v66, v86, v87
	v_cvt_pk_bf16_f32 v67, v88, v89
	v_pk_max_i16 v66, v66, 0
	v_pk_max_i16 v67, v67, 0
	v_pk_max_i16 v68, v68, 0
	v_pk_max_i16 v69, v69, 0
	v_cvt_pk_bf16_f32 v70, v70, v71
	v_cvt_pk_bf16_f32 v71, v72, v73
	s_waitcnt lgkmcnt(1)
	v_mfma_f32_32x32x16_bf16 v[2:17], v[102:105], v[66:69], v[2:17]
	v_cvt_pk_bf16_f32 v72, v74, v75
	v_cvt_pk_bf16_f32 v73, v76, v77
	ds_read_b128 v[74:77], v212 offset:18432
	v_cvt_pk_bf16_f32 v86, v94, v95
	v_cvt_pk_bf16_f32 v87, v96, v97
	v_cvt_pk_bf16_f32 v88, v98, v99
	s_waitcnt lgkmcnt(1)
	v_mfma_f32_32x32x16_bf16 v[50:65], v[90:93], v[66:69], v[50:65]
	ds_read_b128 v[66:69], v212 offset:26624
	v_cvt_pk_bf16_f32 v89, v100, v101
	v_pk_max_i16 v86, v86, 0
	v_pk_max_i16 v87, v87, 0
	v_pk_max_i16 v88, v88, 0
	v_pk_max_i16 v89, v89, 0
	v_pk_max_i16 v70, v70, 0
	v_pk_max_i16 v71, v71, 0
	v_pk_max_i16 v72, v72, 0
	v_pk_max_i16 v73, v73, 0
	v_cvt_pk_bf16_f32 v78, v78, v79
	v_cvt_pk_bf16_f32 v79, v80, v81
	s_waitcnt lgkmcnt(1)
	v_mfma_f32_32x32x16_bf16 v[2:17], v[74:77], v[86:89], v[2:17]
	v_cvt_pk_bf16_f32 v80, v82, v83
	v_cvt_pk_bf16_f32 v81, v84, v85
	v_pk_max_i16 v78, v78, 0
	v_pk_max_i16 v79, v79, 0
	v_pk_max_i16 v80, v80, 0
	v_pk_max_i16 v81, v81, 0
	s_waitcnt lgkmcnt(0)
	v_mfma_f32_32x32x16_bf16 v[50:65], v[66:69], v[86:89], v[50:65]
	v_mfma_f32_32x32x16_bf16 v[34:49], v[90:93], v[70:73], v[34:49]
	s_nop 10
	v_add_f32_e32 v130, v10, v58
	v_add_f32_e32 v131, v11, v59
	v_add_f32_e32 v132, v12, v60
	v_add_f32_e32 v133, v13, v61
	v_add_f32_e32 v138, v4, v52
	v_add_f32_e32 v139, v5, v53
	v_pk_add_f32 v[140:141], v[16:17], v[64:65]
	v_pk_add_f32 v[142:143], v[8:9], v[56:57]
	v_pk_add_f32 v[144:145], v[14:15], v[62:63]
	v_pk_add_f32 v[146:147], v[6:7], v[54:55]
	v_mfma_f32_32x32x16_bf16 v[18:33], v[102:105], v[70:73], v[18:33]
	ds_read2st64_b32 v[70:71], v135 offset0:133 offset1:134
	v_add_f32_e32 v148, v2, v50
	v_add_f32_e32 v149, v3, v51
	v_add_f32_e32 v144, v146, v144
	v_add_f32_e32 v145, v147, v145
	v_pk_add_f32 v[140:141], v[142:143], v[140:141]
	v_pk_add_f32 v[132:133], v[138:139], v[132:133]
	v_pk_add_f32 v[130:131], v[148:149], v[130:131]
	v_pk_add_f32 v[132:133], v[132:133], v[140:141]
	v_pk_add_f32 v[130:131], v[130:131], v[144:145]
	v_mfma_f32_32x32x16_bf16 v[34:49], v[66:69], v[78:81], v[34:49]
	s_waitcnt vmcnt(0) lgkmcnt(0)
	v_mul_f32_e32 v66, v175, v70
	v_add_f32_e32 v130, v131, v130
	v_add_f32_e32 v131, v132, v133
	ds_write_b32 v173, v66 offset:512
	v_mul_f32_e32 v66, v175, v71
	v_add_f32_e32 v130, v130, v131
	s_waitcnt lgkmcnt(0)
	ds_read_b128 v[102:105], v174 offset:34560
	ds_read_b128 v[98:101], v174 offset:34592
	ds_read_b128 v[110:113], v174 offset:34624
	ds_read_b128 v[106:109], v174 offset:34656
	ds_read_b128 v[114:117], v174 offset:34688
	ds_read_b128 v[122:125], v174 offset:34720
	ds_read_b128 v[118:121], v174 offset:34752
	ds_read_b128 v[126:129], v174 offset:34784
	v_mov_b32_dpp v66, v66 quad_perm:[1,0,3,2] row_mask:0xf bank_mask:0xf bound_ctrl:1
	v_mov_b32_e32 v131, v130
	v_fmac_f32_e32 v66, v175, v71
	s_nop 0
	v_permlane32_swap_b32_e32 v130, v131
	v_add_f32_dpp v66, v66, v66 quad_perm:[2,3,0,1] row_mask:0xf bank_mask:0xf bound_ctrl:1
	v_add_f32_e32 v130, v130, v131
	v_fmamk_f32 v65, v130, 0xbc800000, v65
	v_add_f32_dpp v66, v66, v66 row_half_mirror row_mask:0xf bank_mask:0xf bound_ctrl:1
	v_fmamk_f32 v64, v130, 0xbc800000, v64
	v_fmamk_f32 v63, v130, 0xbc800000, v63
	v_fmamk_f32 v62, v130, 0xbc800000, v62
	v_fmamk_f32 v61, v130, 0xbc800000, v61
	v_fmamk_f32 v60, v130, 0xbc800000, v60
	v_fmamk_f32 v59, v130, 0xbc800000, v59
	v_fmamk_f32 v58, v130, 0xbc800000, v58
	v_fmamk_f32 v57, v130, 0xbc800000, v57
	v_fmamk_f32 v56, v130, 0xbc800000, v56
	v_fmamk_f32 v55, v130, 0xbc800000, v55
	v_fmamk_f32 v54, v130, 0xbc800000, v54
	v_fmamk_f32 v53, v130, 0xbc800000, v53
	v_fmamk_f32 v52, v130, 0xbc800000, v52
	v_fmamk_f32 v51, v130, 0xbc800000, v51
	v_fmac_f32_e32 v50, 0xbc800000, v130
	v_add_f32_dpp v66, v66, v66 row_ror:8 row_mask:0xf bank_mask:0xf bound_ctrl:1
	v_fmamk_f32 v17, v130, 0xbc800000, v17
	v_fmamk_f32 v16, v130, 0xbc800000, v16
	v_fmamk_f32 v15, v130, 0xbc800000, v15
	v_fmamk_f32 v14, v130, 0xbc800000, v14
	v_fmamk_f32 v13, v130, 0xbc800000, v13
	v_fmamk_f32 v12, v130, 0xbc800000, v12
	v_fmamk_f32 v11, v130, 0xbc800000, v11
	v_fmamk_f32 v10, v130, 0xbc800000, v10
	v_fmamk_f32 v9, v130, 0xbc800000, v9
	v_fmamk_f32 v8, v130, 0xbc800000, v8
	v_fmamk_f32 v7, v130, 0xbc800000, v7
	v_fmamk_f32 v6, v130, 0xbc800000, v6
	v_fmamk_f32 v5, v130, 0xbc800000, v5
	v_fmamk_f32 v4, v130, 0xbc800000, v4
	v_fmamk_f32 v3, v130, 0xbc800000, v3
	v_fmac_f32_e32 v2, 0xbc800000, v130
	v_pk_mul_f32 v[130:131], v[54:55], v[54:55]
	v_pk_mul_f32 v[132:133], v[62:63], v[62:63]
	v_pk_mul_f32 v[138:139], v[50:51], v[50:51]
	v_pk_mul_f32 v[140:141], v[58:59], v[58:59]
	v_pk_mul_f32 v[142:143], v[56:57], v[56:57]
	v_pk_mul_f32 v[144:145], v[64:65], v[64:65]
	v_pk_mul_f32 v[146:147], v[52:53], v[52:53]
	v_pk_mul_f32 v[148:149], v[60:61], v[60:61]
	v_mov_b32_e32 v67, v66
	v_pk_fma_f32 v[148:149], v[12:13], v[12:13], v[148:149]
	v_pk_fma_f32 v[146:147], v[4:5], v[4:5], v[146:147]
	v_pk_fma_f32 v[144:145], v[16:17], v[16:17], v[144:145]
	v_pk_fma_f32 v[142:143], v[8:9], v[8:9], v[142:143]
	v_pk_fma_f32 v[140:141], v[10:11], v[10:11], v[140:141]
	v_pk_fma_f32 v[138:139], v[2:3], v[2:3], v[138:139]
	v_pk_fma_f32 v[132:133], v[14:15], v[14:15], v[132:133]
	v_pk_fma_f32 v[130:131], v[6:7], v[6:7], v[130:131]
	v_permlane16_swap_b32_e32 v66, v67
	v_pk_add_f32 v[130:131], v[130:131], v[132:133]
	v_pk_add_f32 v[132:133], v[138:139], v[140:141]
	v_pk_add_f32 v[138:139], v[142:143], v[144:145]
	v_pk_add_f32 v[140:141], v[146:147], v[148:149]
	v_mfma_f32_32x32x16_bf16 v[18:33], v[74:77], v[78:81], v[18:33]
	v_add_f32_e32 v136, v66, v67
	ds_read_b128 v[70:73], v134 offset:512
	ds_read_b128 v[66:69], v134 offset:544
	ds_read_b128 v[78:81], v134 offset:576
	ds_read_b128 v[74:77], v134 offset:608
	ds_read_b128 v[82:85], v134 offset:640
	ds_read_b128 v[90:93], v134 offset:672
	ds_read_b128 v[86:89], v134 offset:704
	ds_read_b128 v[94:97], v134 offset:736
	v_pk_add_f32 v[138:139], v[140:141], v[138:139]
	v_pk_add_f32 v[130:131], v[132:133], v[130:131]
	s_waitcnt lgkmcnt(8)
	v_pk_mul_f32 v[140:141], v[126:127], v[62:63]
	v_pk_mov_b32 v[132:133], v[130:131], v[138:139] op_sel:[1,0]
	v_mov_b32_e32 v131, v139
	v_pk_mul_f32 v[138:139], v[122:123], v[54:55]
	v_pk_mul_f32 v[142:143], v[114:115], v[50:51]
	v_pk_mul_f32 v[144:145], v[118:119], v[58:59]
	v_pk_mul_f32 v[146:147], v[124:125], v[56:57]
	v_pk_mul_f32 v[148:149], v[128:129], v[64:65]
	v_pk_mul_f32 v[154:155], v[116:117], v[52:53]
	v_pk_mul_f32 v[156:157], v[120:121], v[60:61]
	v_pk_fma_f32 v[154:155], v[104:105], v[4:5], v[154:155]
	v_pk_fma_f32 v[156:157], v[112:113], v[12:13], v[156:157]
	v_pk_fma_f32 v[148:149], v[108:109], v[16:17], v[148:149]
	v_pk_fma_f32 v[146:147], v[100:101], v[8:9], v[146:147]
	v_pk_fma_f32 v[144:145], v[110:111], v[10:11], v[144:145]
	v_pk_fma_f32 v[142:143], v[102:103], v[2:3], v[142:143]
	v_pk_fma_f32 v[140:141], v[106:107], v[14:15], v[140:141]
	v_pk_fma_f32 v[138:139], v[98:99], v[6:7], v[138:139]
	v_pk_add_f32 v[130:131], v[132:133], v[130:131]
	v_pk_add_f32 v[138:139], v[138:139], v[140:141]
	v_pk_add_f32 v[140:141], v[142:143], v[144:145]
	v_pk_add_f32 v[142:143], v[146:147], v[148:149]
	v_pk_add_f32 v[144:145], v[154:155], v[156:157]
	v_pk_add_f32 v[132:133], v[130:131], v[130:131] op_sel:[0,1] op_sel_hi:[1,0]
	v_pk_add_f32 v[142:143], v[144:145], v[142:143]
	v_pk_add_f32 v[138:139], v[140:141], v[138:139]
	v_add_f32_e32 v133, v142, v143
	v_add_f32_e32 v130, v138, v139
	s_waitcnt lgkmcnt(2)
	v_pk_mul_f32 v[138:139], v[90:91], v[54:55]
	s_waitcnt lgkmcnt(0)
	v_pk_mul_f32 v[140:141], v[94:95], v[62:63]
	v_pk_mul_f32 v[142:143], v[82:83], v[50:51]
	v_pk_mul_f32 v[144:145], v[86:87], v[58:59]
	v_pk_mul_f32 v[146:147], v[92:93], v[56:57]
	v_pk_mul_f32 v[148:149], v[96:97], v[64:65]
	v_pk_mul_f32 v[154:155], v[84:85], v[52:53]
	v_pk_mul_f32 v[156:157], v[88:89], v[60:61]
	v_add_f32_e32 v130, v130, v133
	v_pk_fma_f32 v[156:157], v[80:81], v[12:13], v[156:157]
	v_pk_fma_f32 v[154:155], v[72:73], v[4:5], v[154:155]
	v_pk_fma_f32 v[148:149], v[76:77], v[16:17], v[148:149]
	v_pk_fma_f32 v[146:147], v[68:69], v[8:9], v[146:147]
	v_pk_fma_f32 v[144:145], v[78:79], v[10:11], v[144:145]
	v_pk_fma_f32 v[142:143], v[70:71], v[2:3], v[142:143]
	v_pk_fma_f32 v[140:141], v[74:75], v[14:15], v[140:141]
	v_pk_fma_f32 v[138:139], v[66:67], v[6:7], v[138:139]
	v_mov_b32_e32 v133, v130
	v_pk_add_f32 v[138:139], v[138:139], v[140:141]
	v_pk_add_f32 v[140:141], v[142:143], v[144:145]
	v_pk_add_f32 v[142:143], v[146:147], v[148:149]
	v_pk_add_f32 v[144:145], v[154:155], v[156:157]
	v_permlane32_swap_b32_e32 v130, v133
	v_pk_add_f32 v[142:143], v[144:145], v[142:143]
	v_add_f32_e32 v160, v130, v133
	v_pk_add_f32 v[138:139], v[140:141], v[138:139]
	v_add_f32_e32 v133, v142, v143
	v_pk_add_f32 v[140:141], v[26:27], v[42:43]
	v_pk_add_f32 v[142:143], v[28:29], v[44:45]
	v_pk_add_f32 v[144:145], v[20:21], v[36:37]
	v_pk_add_f32 v[146:147], v[32:33], v[48:49]
	v_pk_add_f32 v[148:149], v[24:25], v[40:41]
	v_pk_add_f32 v[154:155], v[30:31], v[46:47]
	v_pk_add_f32 v[156:157], v[22:23], v[38:39]
	v_pk_add_f32 v[158:159], v[18:19], v[34:35]
	v_pk_add_f32 v[154:155], v[156:157], v[154:155]
	v_pk_add_f32 v[146:147], v[148:149], v[146:147]
	v_pk_add_f32 v[142:143], v[144:145], v[142:143]
	v_pk_add_f32 v[140:141], v[158:159], v[140:141]
	v_pk_add_f32 v[142:143], v[142:143], v[146:147]
	v_pk_add_f32 v[140:141], v[140:141], v[154:155]
	v_add_f32_e32 v130, v138, v139
	v_add_f32_e32 v140, v141, v140
	v_add_f32_e32 v141, v142, v143
	v_add_f32_e32 v133, v130, v133
	v_add_f32_e32 v140, v140, v141
	v_mov_b32_e32 v131, v132
	v_mov_b32_e32 v130, v140
	s_nop 1
	v_permlane32_swap_b32_e32 v140, v130
	v_add_f32_e32 v130, v140, v130
	v_fmamk_f32 v49, v130, 0xbc800000, v49
	v_fmamk_f32 v48, v130, 0xbc800000, v48
	v_fmamk_f32 v47, v130, 0xbc800000, v47
	v_fmamk_f32 v46, v130, 0xbc800000, v46
	v_fmamk_f32 v45, v130, 0xbc800000, v45
	v_fmamk_f32 v44, v130, 0xbc800000, v44
	v_fmamk_f32 v43, v130, 0xbc800000, v43
	v_fmamk_f32 v42, v130, 0xbc800000, v42
	v_fmamk_f32 v41, v130, 0xbc800000, v41
	v_fmamk_f32 v40, v130, 0xbc800000, v40
	v_fmamk_f32 v39, v130, 0xbc800000, v39
	v_fmamk_f32 v38, v130, 0xbc800000, v38
	v_fmamk_f32 v37, v130, 0xbc800000, v37
	v_fmamk_f32 v36, v130, 0xbc800000, v36
	v_fmamk_f32 v35, v130, 0xbc800000, v35
	v_fmac_f32_e32 v34, 0xbc800000, v130
	v_fmamk_f32 v33, v130, 0xbc800000, v33
	v_fmamk_f32 v32, v130, 0xbc800000, v32
	v_fmamk_f32 v31, v130, 0xbc800000, v31
	v_fmamk_f32 v30, v130, 0xbc800000, v30
	v_fmamk_f32 v29, v130, 0xbc800000, v29
	v_fmamk_f32 v28, v130, 0xbc800000, v28
	v_fmamk_f32 v27, v130, 0xbc800000, v27
	v_fmamk_f32 v26, v130, 0xbc800000, v26
	v_fmamk_f32 v25, v130, 0xbc800000, v25
	v_fmamk_f32 v24, v130, 0xbc800000, v24
	v_fmamk_f32 v23, v130, 0xbc800000, v23
	v_fmamk_f32 v22, v130, 0xbc800000, v22
	v_fmamk_f32 v21, v130, 0xbc800000, v21
	v_fmamk_f32 v20, v130, 0xbc800000, v20
	v_fmamk_f32 v19, v130, 0xbc800000, v19
	v_fmac_f32_e32 v18, 0xbc800000, v130
	v_pk_mul_f32 v[140:141], v[38:39], v[38:39]
	v_pk_mul_f32 v[142:143], v[46:47], v[46:47]
	v_pk_mul_f32 v[144:145], v[34:35], v[34:35]
	v_pk_mul_f32 v[146:147], v[42:43], v[42:43]
	v_pk_mul_f32 v[148:149], v[40:41], v[40:41]
	v_pk_mul_f32 v[154:155], v[48:49], v[48:49]
	v_pk_mul_f32 v[156:157], v[36:37], v[36:37]
	v_pk_mul_f32 v[158:159], v[44:45], v[44:45]
	v_pk_fma_f32 v[156:157], v[20:21], v[20:21], v[156:157]
	v_pk_fma_f32 v[158:159], v[28:29], v[28:29], v[158:159]
	v_pk_fma_f32 v[154:155], v[32:33], v[32:33], v[154:155]
	v_pk_fma_f32 v[148:149], v[24:25], v[24:25], v[148:149]
	v_pk_fma_f32 v[146:147], v[26:27], v[26:27], v[146:147]
	v_pk_fma_f32 v[144:145], v[18:19], v[18:19], v[144:145]
	v_pk_fma_f32 v[142:143], v[30:31], v[30:31], v[142:143]
	v_pk_fma_f32 v[140:141], v[22:23], v[22:23], v[140:141]
	v_permlane32_swap_b32_e32 v132, v131
	v_pk_add_f32 v[140:141], v[140:141], v[142:143]
	v_pk_add_f32 v[142:143], v[144:145], v[146:147]
	v_pk_add_f32 v[144:145], v[148:149], v[154:155]
	v_pk_add_f32 v[146:147], v[156:157], v[158:159]
	v_pk_add_f32 v[140:141], v[142:143], v[140:141]
	v_pk_add_f32 v[144:145], v[146:147], v[144:145]
	v_pk_mul_f32 v[122:123], v[122:123], v[38:39]
	v_pk_mov_b32 v[142:143], v[140:141], v[144:145] op_sel:[1,0]
	v_mov_b32_e32 v141, v145
	v_pk_add_f32 v[140:141], v[142:143], v[140:141]
	v_pk_mul_f32 v[126:127], v[126:127], v[46:47]
	v_pk_add_f32 v[140:141], v[140:141], v[140:141] op_sel:[0,1] op_sel_hi:[1,0]
	v_pk_mul_f32 v[114:115], v[114:115], v[34:35]
	v_mov_b32_e32 v130, v140
	s_nop 1
	v_permlane32_swap_b32_e32 v140, v130
	v_mov_b32_e32 v141, v132
	v_pk_add_f32 v[130:131], v[140:141], v[130:131]
	v_pk_mul_f32 v[118:119], v[118:119], v[42:43]
	v_pk_fma_f32 v[130:131], v[130:131], s[0:1], v[152:153] op_sel_hi:[1,0,0]
	v_pk_mul_f32 v[124:125], v[124:125], v[40:41]
	v_pk_mul_f32 v[128:129], v[128:129], v[48:49]
	v_pk_mul_f32 v[116:117], v[116:117], v[36:37]
	v_pk_mul_f32 v[120:121], v[120:121], v[44:45]
	v_pk_fma_f32 v[112:113], v[112:113], v[28:29], v[120:121]
	v_pk_fma_f32 v[104:105], v[104:105], v[20:21], v[116:117]
	v_pk_fma_f32 v[108:109], v[108:109], v[32:33], v[128:129]
	v_pk_fma_f32 v[100:101], v[100:101], v[24:25], v[124:125]
	v_pk_fma_f32 v[110:111], v[110:111], v[26:27], v[118:119]
	v_pk_fma_f32 v[102:103], v[102:103], v[18:19], v[114:115]
	v_pk_fma_f32 v[106:107], v[106:107], v[30:31], v[126:127]
	v_pk_fma_f32 v[98:99], v[98:99], v[22:23], v[122:123]
	v_rsq_f32_e32 v131, v131
	v_pk_add_f32 v[98:99], v[98:99], v[106:107]
	v_pk_add_f32 v[102:103], v[102:103], v[110:111]
	v_pk_add_f32 v[100:101], v[100:101], v[108:109]
	v_pk_add_f32 v[104:105], v[104:105], v[112:113]
	v_rsq_f32_e32 v132, v130
	v_pk_add_f32 v[100:101], v[104:105], v[100:101]
	v_pk_add_f32 v[98:99], v[102:103], v[98:99]
	v_add_f32_e32 v98, v98, v99
	v_add_f32_e32 v99, v100, v101
	v_add_f32_e32 v98, v98, v99
	v_mov_b32_e32 v99, v98
	v_pk_mul_f32 v[90:91], v[90:91], v[38:39]
	v_pk_mul_f32 v[94:95], v[94:95], v[46:47]
	v_pk_mul_f32 v[82:83], v[82:83], v[34:35]
	v_pk_mul_f32 v[86:87], v[86:87], v[42:43]
	v_permlane32_swap_b32_e32 v98, v99
	v_pk_fma_f32 v[78:79], v[78:79], v[26:27], v[86:87]
	v_pk_fma_f32 v[70:71], v[70:71], v[18:19], v[82:83]
	v_pk_fma_f32 v[74:75], v[74:75], v[30:31], v[94:95]
	v_pk_fma_f32 v[66:67], v[66:67], v[22:23], v[90:91]
	v_mov_b32_e32 v130, v131
	v_mov_b32_e32 v131, v132
	v_add_f32_e32 v98, v98, v99
	v_pk_add_f32 v[66:67], v[66:67], v[74:75]
	v_pk_add_f32 v[70:71], v[70:71], v[78:79]
	v_mul_f32_e32 v139, v160, v130
	v_mul_f32_e32 v98, v98, v131
	v_pk_add_f32 v[66:67], v[70:71], v[66:67]
	v_cmp_gt_u32_e32 vcc, 32, v1
	v_add_f32_e32 v66, v66, v67
	v_pk_mul_f32 v[92:93], v[92:93], v[40:41]
	v_cndmask_b32_e32 v67, v98, v139, vcc
	v_add_f32_e32 v67, s12, v67
	v_pk_mul_f32 v[96:97], v[96:97], v[48:49]
	v_pk_mul_f32 v[84:85], v[84:85], v[36:37]
	v_pk_mul_f32 v[88:89], v[88:89], v[44:45]
	v_mul_f32_e32 v67, 0xbfb8aa3b, v67
	v_pk_fma_f32 v[80:81], v[80:81], v[28:29], v[88:89]
	v_pk_fma_f32 v[72:73], v[72:73], v[20:21], v[84:85]
	v_pk_fma_f32 v[76:77], v[76:77], v[32:33], v[96:97]
	v_pk_fma_f32 v[68:69], v[68:69], v[24:25], v[92:93]
	v_exp_f32_e32 v70, v67
	v_pk_add_f32 v[68:69], v[68:69], v[76:77]
	v_pk_add_f32 v[72:73], v[72:73], v[80:81]
	v_cmp_lt_i32_e64 s[0:1], 0, v151
	v_pk_add_f32 v[68:69], v[72:73], v[68:69]
	v_mov_b32_e32 v137, v136
	v_add_f32_e32 v67, v68, v69
	v_add_f32_e32 v67, v66, v67
	v_add_f32_e32 v66, 1.0, v70
	v_rcp_f32_e32 v66, v66
	v_mov_b32_e32 v69, 0xff800000
	v_mov_b32_e32 v138, v133
	v_mov_b32_e32 v68, v67
	v_cndmask_b32_e64 v70, v69, v66, s[0:1]
	v_mbcnt_lo_u32_b32 v66, -1, 0
	v_mbcnt_hi_u32_b32 v66, -1, v66
	v_permlane32_swap_b32_e32 v136, v137
	v_permlane32_swap_b32_e32 v133, v138
	v_permlane32_swap_b32_e32 v67, v68
	v_and_b32_e32 v86, 64, v66
	s_mov_b32 s14, 8
	s_mov_b32 s13, 0
	v_mov_b32_e32 v66, 0
	s_waitcnt lgkmcnt(0)
